# MLA loop: the WAR barrier at the end of the second-half step moved to just before the next tile's LDS write (waves may start the next QK before the rendezvous); plus static prio
# speedup vs baseline: 1.0019x; 1.0019x over previous
.LBB0_565:
	s_waitcnt lgkmcnt(4)
	v_mfma_scale_f32_32x32x64_f8f6f4 v[96:111], v[96:103], v[120:127], 0, v205, v205 op_sel_hi:[0,0,0]
	v_cndmask_b32_e64 v176, v189, v192, s[4:5]
	v_fma_f32 v80, v80, s40, -v176
	v_fma_f32 v81, v81, s40, -v176
	v_fma_f32 v84, v84, s40, -v176
	v_fma_f32 v85, v85, s40, -v176
	v_fma_f32 v88, v88, s40, -v176
	v_fma_f32 v89, v89, s40, -v176
	v_fma_f32 v92, v92, s40, -v176
	v_fma_f32 v93, v93, s40, -v176
	v_exp_f32_e32 v80, v80
	v_exp_f32_e32 v81, v81
	v_exp_f32_e32 v84, v84
	v_exp_f32_e32 v85, v85
	v_exp_f32_e32 v88, v88
	v_exp_f32_e32 v89, v89
	s_waitcnt lgkmcnt(2)
	v_mfma_scale_f32_32x32x64_f8f6f4 v[96:111], v[156:163], v[128:135], v[96:111], v205, v205 op_sel_hi:[0,0,0]
	v_exp_f32_e32 v92, v92
	v_exp_f32_e32 v93, v93
	v_fma_f32 v82, v82, s40, -v176
	v_fma_f32 v83, v83, s40, -v176
	v_fma_f32 v86, v86, s40, -v176
	v_fma_f32 v87, v87, s40, -v176
	v_fma_f32 v90, v90, s40, -v176
	v_fma_f32 v91, v91, s40, -v176
	v_fma_f32 v94, v94, s40, -v176
	v_fma_f32 v95, v95, s40, -v176
	v_exp_f32_e32 v82, v82
	v_exp_f32_e32 v83, v83
	v_exp_f32_e32 v86, v86
	v_exp_f32_e32 v87, v87
	v_exp_f32_e32 v90, v90
	s_waitcnt lgkmcnt(0)
	v_mfma_scale_f32_32x32x64_f8f6f4 v[96:111], v[148:155], v[136:143], v[96:111], v205, v205 op_sel_hi:[0,0,0]
	v_mov_b32_e32 v148, 0
	v_mov_b32_e32 v149, 0
	v_mov_b32_e32 v150, 0
	v_mov_b32_e32 v151, 0
	v_exp_f32_e32 v91, v91
	v_exp_f32_e32 v94, v94
	v_exp_f32_e32 v95, v95
	v_cvt_pk_fp8_f32 v148, v80, v81
	v_cvt_pk_fp8_f32 v149, v84, v85
	v_cvt_pk_fp8_f32 v150, v88, v89
	v_cvt_pk_fp8_f32 v151, v92, v93
	v_lshl_add_u32 v156, s23, 14, v211
	v_cvt_pk_fp8_f32 v148, v82, v83 op_sel:[0,0,1]
	v_cvt_pk_fp8_f32 v149, v86, v87 op_sel:[0,0,1]
	v_cvt_pk_fp8_f32 v150, v90, v91 op_sel:[0,0,1]
	v_cvt_pk_fp8_f32 v151, v94, v95 op_sel:[0,0,1]
	ds_read_b128 v[80:83], v156
	ds_read_b128 v[84:87], v156 offset:16
	ds_read_b128 v[88:91], v156 offset:2560
	ds_read_b128 v[92:95], v156 offset:2576
	s_waitcnt lgkmcnt(0)
	s_waitcnt lgkmcnt(2)
	v_mfma_scale_f32_32x32x64_f8f6f4 v[48:63], v[144:151], v[80:87], v[48:63], v205, v205 op_sel_hi:[0,0,0]
	ds_read_b128 v[80:83], v156 offset:5120
	ds_read_b128 v[84:87], v156 offset:5136
	ds_read_b128 v[152:155], v156 offset:7680
	ds_read_b128 v[156:159], v156 offset:7696
	s_waitcnt lgkmcnt(0)
	s_waitcnt lgkmcnt(4)
	v_mfma_scale_f32_32x32x64_f8f6f4 v[32:47], v[144:151], v[88:95], v[32:47], v205, v205 op_sel_hi:[0,0,0]
	v_max_f32_e32 v88, v97, v97
	v_max_f32_e32 v89, v96, v96
	v_max_f32_e32 v88, v89, v88
	v_max3_f32 v88, v88, v98, v99
	v_max3_f32 v88, v88, v100, v101
	v_max3_f32 v88, v88, v102, v103
	v_max3_f32 v88, v88, v104, v105
	v_max3_f32 v88, v88, v106, v107
	s_waitcnt lgkmcnt(2)
	v_mfma_scale_f32_32x32x64_f8f6f4 v[16:31], v[144:151], v[80:87], v[16:31], v205, v205 op_sel_hi:[0,0,0]
	v_max3_f32 v88, v88, v108, v109
	v_max3_f32 v88, v88, v110, v111
	v_mov_b32_e32 v89, v88
	s_nop 1
	v_permlane32_swap_b32_e32 v88, v89
	v_max_f32_e32 v80, v89, v89
	v_max_f32_e32 v81, v88, v88
	v_max_f32_e32 v80, v81, v80
	v_fma_f32 v81, v80, s40, -v176
	v_cmp_ge_f32_e32 vcc, s70, v81
	v_fmamk_f32 v80, v80, 0x3dd53b94, v202
	v_max_f32_e32 v81, v176, v176
	v_max_f32_e32 v80, v81, v80
	v_sub_f32_e32 v81, v176, v80
	v_exp_f32_e32 v81, v81
	s_waitcnt lgkmcnt(0)
	v_mfma_scale_f32_32x32x64_f8f6f4 v[0:15], v[144:151], v[152:159], v[0:15], v205, v205 op_sel_hi:[0,0,0]
	s_cmp_eq_u64 vcc, exec
	s_cselect_b64 vcc, -1, 0
	v_cndmask_b32_e32 v192, v80, v176, vcc
	s_add_i32 s21, s21, 2
	s_add_i32 s78, s78, 1
	s_add_i32 s22, s22, 64
	v_fma_f32 v178, v96, s40, -v192
	v_fma_f32 v179, v97, s40, -v192
	v_fma_f32 v176, v98, s40, -v192
	v_fma_f32 v177, v99, s40, -v192
	v_fma_f32 v162, v100, s40, -v192
	v_fma_f32 v163, v101, s40, -v192
	v_fma_f32 v160, v102, s40, -v192
	v_fma_f32 v161, v103, s40, -v192
	v_pk_fma_f32 v[158:159], v[104:105], s[40:41], v[192:193] op_sel_hi:[1,0,0] neg_lo:[0,0,1] neg_hi:[0,0,1]
	v_pk_fma_f32 v[156:157], v[106:107], s[40:41], v[192:193] op_sel_hi:[1,0,0] neg_lo:[0,0,1] neg_hi:[0,0,1]
	v_pk_fma_f32 v[154:155], v[108:109], s[40:41], v[192:193] op_sel_hi:[1,0,0] neg_lo:[0,0,1] neg_hi:[0,0,1]
	v_pk_fma_f32 v[152:153], v[110:111], s[40:41], v[192:193] op_sel_hi:[1,0,0] neg_lo:[0,0,1] neg_hi:[0,0,1]
	v_cndmask_b32_e64 v88, v81, 1.0, vcc
	v_mfma_scale_f32_32x32x64_f8f6f4 v[64:79], v[144:151], v[112:119], v[64:79], v205, v205 op_sel_hi:[0,0,0]
	s_cmp_ge_u32 s21, s17
	s_nop 0
	s_cbranch_scc1 .LBB0_580

.LBB0_570:
	s_waitcnt lgkmcnt(4)
	v_mfma_scale_f32_32x32x64_f8f6f4 v[80:95], v[80:87], v[120:127], 0, v205, v205 op_sel_hi:[0,0,0]
	s_mov_b64 s[4:5], exec
	s_cmp_ge_u32 s18, s20
	s_waitcnt lgkmcnt(2)
	v_mfma_scale_f32_32x32x64_f8f6f4 v[80:95], v[104:111], v[128:135], v[80:95], v205, v205 op_sel_hi:[0,0,0]
	s_waitcnt lgkmcnt(0)
	v_mfma_scale_f32_32x32x64_f8f6f4 v[80:95], v[96:103], v[136:143], v[80:95], v205, v205 op_sel_hi:[0,0,0]
	s_nop 15
	s_nop 3
	v_max_f32_e32 v96, v81, v81
	v_max_f32_e32 v97, v80, v80
	v_max_f32_e32 v96, v97, v96
	v_max3_f32 v96, v96, v82, v83
	v_max3_f32 v96, v96, v84, v85
	v_max3_f32 v96, v96, v86, v87
	v_max3_f32 v96, v96, v88, v89
	v_max3_f32 v96, v96, v90, v91
	v_max3_f32 v96, v96, v92, v93
	v_max3_f32 v96, v96, v94, v95
	v_mov_b32_e32 v97, v96
	s_nop 1
	v_permlane32_swap_b32_e32 v96, v97
	v_max_f32_e32 v97, v97, v97
	v_max_f32_e32 v96, v96, v96
	v_max_f32_e32 v96, v96, v97
	v_fma_f32 v97, v96, s40, -v192
	v_cmp_ge_f32_e32 vcc, s70, v97
	s_barrier
	s_cbranch_scc1 .LBB0_577
	s_xor_b32 s25, s23, 1
	s_lshl_b32 s18, s25, 15
	s_add_i32 s26, s18, 0
	v_add3_u32 v97, s26, v212, v190
	s_waitcnt vmcnt(1)
	ds_write_b128 v97, v[168:171]
	s_and_saveexec_b64 s[18:19], s[0:1]
	v_add3_u32 v97, s26, v215, v188
	ds_write_b128 v97, v[164:167]
	s_or_b64 exec, exec, s[18:19]
	v_lshl_add_u32 v97, s25, 14, v207
	s_cmp_ge_u32 s78, s74
	s_waitcnt vmcnt(0)
	ds_write_b128 v97, v[172:175]
	s_cbranch_scc1 .LBB0_577
	s_cmp_lt_u32 s78, s77
	s_cselect_b32 s18, 0, s77
	s_cselect_b32 s19, s76, s75
	s_lshl_b32 s18, s18, 6
	s_sub_i32 s25, s19, s18
	s_add_i32 s25, s25, s22
	v_add_u32_e32 v97, s25, v210
	v_mad_i64_i32 v[98:99], s[18:19], v97, s64, v[194:195]
	global_load_dwordx4 v[168:171], v[98:99], off
	s_and_saveexec_b64 s[18:19], s[0:1]
	s_cbranch_execz .LBB0_576
	v_add_u32_e32 v97, s25, v213
	v_mad_i64_i32 v[98:99], s[26:27], v97, s64, v[196:197]
	global_load_dwordx4 v[164:167], v[98:99], off

.LBB0_1875:
	s_waitcnt lgkmcnt(4)
	v_mfma_scale_f32_32x32x64_f8f6f4 v[96:111], v[96:103], v[120:127], 0, v207, v207 op_sel_hi:[0,0,0]
	v_cndmask_b32_e64 v176, v191, v194, s[4:5]
	v_fma_f32 v80, v80, s38, -v176
	v_fma_f32 v81, v81, s38, -v176
	v_fma_f32 v84, v84, s38, -v176
	v_fma_f32 v85, v85, s38, -v176
	v_fma_f32 v88, v88, s38, -v176
	v_fma_f32 v89, v89, s38, -v176
	v_fma_f32 v92, v92, s38, -v176
	v_fma_f32 v93, v93, s38, -v176
	v_exp_f32_e32 v80, v80
	v_exp_f32_e32 v81, v81
	v_exp_f32_e32 v84, v84
	v_exp_f32_e32 v85, v85
	v_exp_f32_e32 v88, v88
	v_exp_f32_e32 v89, v89
	s_waitcnt lgkmcnt(2)
	v_mfma_scale_f32_32x32x64_f8f6f4 v[96:111], v[156:163], v[128:135], v[96:111], v207, v207 op_sel_hi:[0,0,0]
	v_exp_f32_e32 v92, v92
	v_exp_f32_e32 v93, v93
	v_fma_f32 v82, v82, s38, -v176
	v_fma_f32 v83, v83, s38, -v176
	v_fma_f32 v86, v86, s38, -v176
	v_fma_f32 v87, v87, s38, -v176
	v_fma_f32 v90, v90, s38, -v176
	v_fma_f32 v91, v91, s38, -v176
	v_fma_f32 v94, v94, s38, -v176
	v_fma_f32 v95, v95, s38, -v176
	v_exp_f32_e32 v82, v82
	v_exp_f32_e32 v83, v83
	v_exp_f32_e32 v86, v86
	v_exp_f32_e32 v87, v87
	v_exp_f32_e32 v90, v90
	s_waitcnt lgkmcnt(0)
	v_mfma_scale_f32_32x32x64_f8f6f4 v[96:111], v[148:155], v[136:143], v[96:111], v207, v207 op_sel_hi:[0,0,0]
	v_mov_b32_e32 v148, 0
	v_mov_b32_e32 v149, 0
	v_mov_b32_e32 v150, 0
	v_mov_b32_e32 v151, 0
	v_exp_f32_e32 v91, v91
	v_exp_f32_e32 v94, v94
	v_exp_f32_e32 v95, v95
	v_cvt_pk_fp8_f32 v148, v80, v81
	v_cvt_pk_fp8_f32 v149, v84, v85
	v_cvt_pk_fp8_f32 v150, v88, v89
	v_cvt_pk_fp8_f32 v151, v92, v93
	v_lshl_add_u32 v156, s24, 14, v209
	v_cvt_pk_fp8_f32 v148, v82, v83 op_sel:[0,0,1]
	v_cvt_pk_fp8_f32 v149, v86, v87 op_sel:[0,0,1]
	v_cvt_pk_fp8_f32 v150, v90, v91 op_sel:[0,0,1]
	v_cvt_pk_fp8_f32 v151, v94, v95 op_sel:[0,0,1]
	ds_read_b128 v[80:83], v156
	ds_read_b128 v[84:87], v156 offset:16
	ds_read_b128 v[88:91], v156 offset:2560
	ds_read_b128 v[92:95], v156 offset:2576
	s_waitcnt lgkmcnt(0)
	s_waitcnt lgkmcnt(2)
	v_mfma_scale_f32_32x32x64_f8f6f4 v[48:63], v[144:151], v[80:87], v[48:63], v207, v207 op_sel_hi:[0,0,0]
	ds_read_b128 v[80:83], v156 offset:5120
	ds_read_b128 v[84:87], v156 offset:5136
	ds_read_b128 v[152:155], v156 offset:7680
	ds_read_b128 v[156:159], v156 offset:7696
	s_waitcnt lgkmcnt(0)
	s_waitcnt lgkmcnt(4)
	v_mfma_scale_f32_32x32x64_f8f6f4 v[32:47], v[144:151], v[88:95], v[32:47], v207, v207 op_sel_hi:[0,0,0]
	v_max_f32_e32 v88, v97, v97
	v_max_f32_e32 v89, v96, v96
	v_max_f32_e32 v88, v89, v88
	v_max3_f32 v88, v88, v98, v99
	v_max3_f32 v88, v88, v100, v101
	v_max3_f32 v88, v88, v102, v103
	v_max3_f32 v88, v88, v104, v105
	v_max3_f32 v88, v88, v106, v107
	s_waitcnt lgkmcnt(2)
	v_mfma_scale_f32_32x32x64_f8f6f4 v[16:31], v[144:151], v[80:87], v[16:31], v207, v207 op_sel_hi:[0,0,0]
	v_max3_f32 v88, v88, v108, v109
	v_max3_f32 v88, v88, v110, v111
	v_mov_b32_e32 v89, v88
	s_nop 1
	v_permlane32_swap_b32_e32 v88, v89
	v_max_f32_e32 v80, v89, v89
	v_max_f32_e32 v81, v88, v88
	v_max_f32_e32 v80, v81, v80
	v_fma_f32 v81, v80, s38, -v176
	v_cmp_ge_f32_e32 vcc, s68, v81
	v_fmamk_f32 v80, v80, 0x3dd53b94, v204
	v_max_f32_e32 v81, v176, v176
	v_max_f32_e32 v80, v81, v80
	v_sub_f32_e32 v81, v176, v80
	v_exp_f32_e32 v81, v81
	s_waitcnt lgkmcnt(0)
	v_mfma_scale_f32_32x32x64_f8f6f4 v[0:15], v[144:151], v[152:159], v[0:15], v207, v207 op_sel_hi:[0,0,0]
	s_cmp_eq_u64 vcc, exec
	s_cselect_b64 vcc, -1, 0
	v_cndmask_b32_e32 v194, v80, v176, vcc
	v_fma_f32 v178, v96, s38, -v194
	v_fma_f32 v179, v97, s38, -v194
	v_fma_f32 v176, v98, s38, -v194
	v_fma_f32 v177, v99, s38, -v194
	v_fma_f32 v162, v100, s38, -v194
	v_fma_f32 v163, v101, s38, -v194
	v_fma_f32 v160, v102, s38, -v194
	v_fma_f32 v161, v103, s38, -v194
	v_fma_f32 v158, v104, s38, -v194
	v_fma_f32 v159, v105, s38, -v194
	v_pk_fma_f32 v[156:157], v[106:107], s[38:39], v[194:195] op_sel_hi:[1,0,0] neg_lo:[0,0,1] neg_hi:[0,0,1]
	v_pk_fma_f32 v[154:155], v[108:109], s[38:39], v[194:195] op_sel_hi:[1,0,0] neg_lo:[0,0,1] neg_hi:[0,0,1]
	v_pk_fma_f32 v[152:153], v[110:111], s[38:39], v[194:195] op_sel_hi:[1,0,0] neg_lo:[0,0,1] neg_hi:[0,0,1]
	v_cndmask_b32_e64 v88, v81, 1.0, vcc
	s_add_i32 s17, s17, 2
	s_add_i32 s76, s76, 1
	s_and_b64 vcc, exec, s[18:19]
	v_mfma_scale_f32_32x32x64_f8f6f4 v[64:79], v[144:151], v[112:119], v[64:79], v207, v207 op_sel_hi:[0,0,0]
	s_nop 0
	s_cbranch_vccnz .LBB0_1889

.LBB0_1880:
	s_waitcnt lgkmcnt(4)
	v_mfma_scale_f32_32x32x64_f8f6f4 v[80:95], v[80:87], v[120:127], 0, v207, v207 op_sel_hi:[0,0,0]
	s_xor_b32 s22, s24, 1
	s_lshl_b32 s18, s22, 15
	s_add_i32 s23, s18, 0
	s_mov_b64 s[20:21], exec
	s_waitcnt lgkmcnt(2)
	v_mfma_scale_f32_32x32x64_f8f6f4 v[80:95], v[104:111], v[128:135], v[80:95], v207, v207 op_sel_hi:[0,0,0]
	s_waitcnt lgkmcnt(0)
	v_mfma_scale_f32_32x32x64_f8f6f4 v[80:95], v[96:103], v[136:143], v[80:95], v207, v207 op_sel_hi:[0,0,0]
	s_nop 15
	s_nop 3
	v_max_f32_e32 v96, v81, v81
	v_max_f32_e32 v97, v80, v80
	v_max_f32_e32 v96, v97, v96
	v_max3_f32 v96, v96, v82, v83
	v_max3_f32 v96, v96, v84, v85
	v_max3_f32 v96, v96, v86, v87
	v_max3_f32 v96, v96, v88, v89
	v_max3_f32 v96, v96, v90, v91
	v_max3_f32 v96, v96, v92, v93
	v_max3_f32 v96, v96, v94, v95
	v_mov_b32_e32 v97, v96
	s_nop 1
	v_permlane32_swap_b32_e32 v96, v97
	v_max_f32_e32 v97, v97, v97
	v_max_f32_e32 v96, v96, v96
	v_max_f32_e32 v96, v96, v97
	v_fma_f32 v97, v96, s38, -v194
	v_cmp_ge_f32_e64 s[4:5], s68, v97
	s_barrier
	v_add3_u32 v97, s23, v210, v190
	s_waitcnt vmcnt(1)
	ds_write_b128 v97, v[168:171]
	s_and_saveexec_b64 s[18:19], s[0:1]
	v_add3_u32 v97, s23, v216, v192
	ds_write_b128 v97, v[164:167]
	s_or_b64 exec, exec, s[18:19]
	s_cmpk_gt_u32 s17, 0x83
	s_cselect_b64 s[18:19], -1, 0
	v_lshl_add_u32 v97, s22, 14, v211
	s_and_b64 vcc, exec, s[18:19]
	s_waitcnt vmcnt(0)
	ds_write_b128 v97, v[172:175]
	s_cbranch_vccnz .LBB0_1886
	s_cmpk_lt_u32 s17, 0x7c
	s_cselect_b32 s22, 0, 0xffffffc0
	s_cselect_b32 s23, s74, s75
	s_add_i32 s22, s22, s76
	s_lshl_b32 s26, s22, 6
	s_add_i32 s26, s26, s23
	v_add_u32_e32 v97, s26, v189
	v_mad_i64_i32 v[98:99], s[22:23], v97, s62, v[196:197]
	global_load_dwordx4 v[168:171], v[98:99], off
	s_and_saveexec_b64 s[22:23], s[0:1]
	s_cbranch_execz .LBB0_1885
	v_add_u32_e32 v97, s26, v212
	v_mad_i64_i32 v[98:99], s[28:29], v97, s62, v[198:199]
	global_load_dwordx4 v[164:167], v[98:99], off
